# sel-attn K/V fragment LDS addresses precomputed per phase (4 regs + immediate offsets); plus bias-address merge and cmp stats-chain restructure
# speedup vs baseline: 1.0021x; 1.0021x over previous
; #define LAS __attribute__((address_space(3)))
;     ...
;     const int lane = c.lane, wave = c.wave, n = lane & 15, q = lane >> 4, hr = n & 3;
;     LAS float* reltab = (LAS float*)(L + A_REL);
;     if (load_rel) { __syncthreads();
;     reltab[c.tid] = inptr(c, I_REL)[c.tid]; }
;     ...
;                         if (MODE == 3) {
; #pragma unroll
;                             for (int kt = 0; kt < 4; ++kt)
; #pragma unroll
;                                 for (int ks = 0; ks < 2; ++ks) akq[kt][ks] = *(const LAS bf16x8*)(L + LK + (16 * kt + n) * 128 + ((((4 * ks + q) ^ n) & 7) << 4));
;                             if (!far) { const LAS float* tp = biasd + hr * NT + (DOFF - tq + p0) + 4 * q;
; #pragma unroll
;                                 for (int kt = 0; kt < 4; ++kt)
; #pragma unroll
;                                     for (int r = 0; r < 4; ++r) bia[kt][r] = tp[16 * kt + r]; }
;                             __builtin_amdgcn_sched_barrier(0);
;                         }
; #pragma unroll
;                         for (int kt = 0; kt < 4; ++kt) { sc[kt] = (f32x4){0.f, 0.f, 0.f, 0.f};
; #pragma unroll
;                             for (int ks = 0; ks < 2; ++ks) { const bf16x8 ak = (MODE != 3) ? akf[kt][ks] : akq[kt][ks];
;                                 sc[kt] = __builtin_amdgcn_mfma_f32_16x16x32_bf16(ak, Bq[qd][ks], sc[kt], 0, 0, 0); } }
;                         if (MODE == 3) {
; #pragma unroll
;                             for (int st = 0; st < 2; ++st)
; #pragma unroll
;                                 for (int dt = 0; dt < 4; ++dt) avq[st][dt] = *(const LAS bf16x8*)(L + LV + (16 * dt + n) * 128 + ((((4 * st + q) ^ n) & 7) << 4));
.LBB0_1117:
	v_readlane_b32 s0, v253, 24
	s_waitcnt vmcnt(0)
	s_barrier
	v_mov_b32_e32 v0, s0
	v_readlane_b32 s0, v253, 25
	s_nop 1
	v_mov_b32_e32 v2, s0
	s_barrier
	ds_read_b32 v0, v0
	ds_read_b32 v2, v2
	v_ashrrev_i32_e32 v155, 31, v154
	s_cmpk_gt_i32 s20, 0x1ff
	s_waitcnt lgkmcnt(1)
	v_readfirstlane_b32 s0, v0
	s_waitcnt lgkmcnt(0)
	v_readfirstlane_b32 s1, v2
	v_mov_b32_e32 v2, s0
	v_readfirstlane_b32 s0, v154
	v_mov_b32_e32 v3, s1
	v_lshl_add_u64 v[2:3], v[154:155], 2, v[2:3]
	flat_load_dword v0, v[2:3]
	v_lshl_add_u32 v2, v154, 2, 0
	v_add_u32_e32 v2, 0x25500, v2
	s_waitcnt vmcnt(0) lgkmcnt(0)
	ds_write_b32 v2, v0
	s_cbranch_scc1 .LBB0_1311
	v_and_b32_e32 v4, 63, v154
	v_and_b32_e32 v6, 15, v154
	v_bfe_u32 v5, v154, 4, 2
	v_cmp_gt_u32_e64 s[36:37], 8, v4
	v_and_b32_e32 v4, 7, v154
	v_lshlrev_b32_e32 v6, 7, v6
	s_add_i32 s26, 0, 0x12000
	s_add_i32 s27, 0, 0x16000
	s_add_i32 s28, 0, 0x1a000
	v_lshlrev_b32_e32 v2, 3, v5
	v_add_u32_e32 v187, 0, v6
	v_lshlrev_b32_e32 v189, 2, v5
	v_xor_b32_e32 v5, v5, v154
	v_add_u32_e32 v207, s26, v6
	v_add_u32_e32 v212, s27, v6
	v_add_u32_e32 v217, s28, v6
	v_ashrrev_i32_e32 v221, 3, v154
	v_lshlrev_b32_e32 v6, 3, v4
	v_lshlrev_b32_e32 v5, 4, v5
	v_mov_b32_e32 v8, 0x70
	v_lshl_or_b32 v158, v221, 12, v6
	v_lshl_or_b32 v160, v221, 14, v6
	v_lshlrev_b32_e32 v6, 1, v154
	v_and_b32_e32 v195, 0x70, v5
	v_bitop3_b32 v204, v5, 64, v8 bitop3:0x6c
	v_lshlrev_b32_e32 v5, 2, v154
	v_xor_b32_e32 v9, v221, v154
	v_and_b32_e32 v10, 4, v154
	v_and_b32_e32 v6, 2, v6
	v_and_b32_e32 v11, 7, v221
	v_lshlrev_b32_e32 v9, 4, v9
	v_bitop3_b32 v6, v6, v11, v10 bitop3:0x36
	v_and_b32_e32 v10, 8, v5
	v_lshlrev_b32_e32 v8, 7, v221
	v_and_b32_e32 v9, 0x70, v9
	v_lshl_or_b32 v6, v6, 4, v10
	v_or_b32_e32 v224, v6, v8
	v_add3_u32 v228, 0, v8, v9
	v_bitop3_b32 v229, v6, 16, v8 bitop3:0x36
	v_and_b32_e32 v8, 64, v244
	v_xor_b32_e32 v6, 16, v244
	v_add_u32_e32 v8, 64, v8
	v_cmp_lt_i32_e32 vcc, v6, v8
	s_ashr_i32 s0, s0, 3
	v_and_b32_e32 v156, 3, v154
	v_cndmask_b32_e32 v6, v244, v6, vcc
	v_lshlrev_b32_e32 v230, 2, v6
	v_xor_b32_e32 v6, 32, v244
	v_bfi_b32 v7, -8, s0, v154
	v_readlane_b32 s1, v253, 32
	v_ashrrev_i32_e32 v226, 5, v154
	v_cmp_lt_i32_e32 vcc, v6, v8
	v_mul_u32_u24_e32 v3, 0x1220, v156
	s_and_b32 s21, s0, -8
	v_bfe_u32 v155, v154, 2, 2
	v_lshlrev_b32_e32 v0, 6, v156
	v_lshl_add_u32 v157, v7, 5, s1
	s_add_i32 s0, 0, 0x20000
	v_and_b32_e32 v7, 48, v154
	v_add_u32_e32 v222, s1, v5
	v_readlane_b32 s2, v253, 33
	s_movk_i32 s1, 0x1220
	v_lshlrev_b32_e64 v10, v154, -1
	v_cndmask_b32_e32 v6, v244, v6, vcc
	v_and_b32_e32 v232, 0x7ffffffc, v226
	v_lshlrev_b32_e64 v191, v155, 1
	v_lshlrev_b32_e64 v205, v155, 16
	v_add_u32_e32 v206, v187, v195
	v_add_u32_e32 v208, v187, v204
	v_add_u32_e32 v209, 0x10000, v206
	v_add_u32_e32 v210, 0x10000, v208
	v_cmp_gt_i32_e64 s[38:39], 8, v154
	v_lshl_add_u32 v223, v4, 2, s2
	v_cmp_gt_i32_e64 s[6:7], s23, v154
	v_cmp_eq_u32_e64 s[8:9], 0, v154
	v_cmp_gt_i32_e64 s[10:11], s1, v154
	v_add_u32_e32 v225, s2, v5
	v_not_b32_e32 v227, v10
	v_cmp_lt_i32_e64 s[46:47], 0, v226
	v_mov_b32_e32 v159, v1
	v_mov_b32_e32 v161, v1
	v_lshlrev_b32_e32 v231, 2, v6
	v_cmp_lt_u32_e64 s[48:49], 3, v226
	v_cmp_ne_u32_e64 s[50:51], v226, v232
	v_add3_u32 v233, s0, v3, v7
	v_add_u32_e32 v234, s0, v5
	v_lshlrev_b32_e32 v0, 1, v0
	v_lshlrev_b32_e32 v162, 1, v2
	v_lshlrev_b32_e32 v164, 1, v156
	v_lshlrev_b32_e32 v166, 2, v4
	s_branch .LBB0_1121

; #define LAS __attribute__((address_space(3)))
;     ...
;                         if (MODE == 3) {
; #pragma unroll
;                             for (int kt = 0; kt < 4; ++kt)
; #pragma unroll
;                                 for (int ks = 0; ks < 2; ++ks) akq[kt][ks] = *(const LAS bf16x8*)(L + LK + (16 * kt + n) * 128 + ((((4 * ks + q) ^ n) & 7) << 4));
;                             if (!far) { const LAS float* tp = biasd + hr * NT + (DOFF - tq + p0) + 4 * q;
; #pragma unroll
;                                 for (int kt = 0; kt < 4; ++kt)
; #pragma unroll
;                                     for (int r = 0; r < 4; ++r) bia[kt][r] = tp[16 * kt + r]; }
;                             __builtin_amdgcn_sched_barrier(0);
;                         }
; #pragma unroll
;                         for (int kt = 0; kt < 4; ++kt) { sc[kt] = (f32x4){0.f, 0.f, 0.f, 0.f};
; #pragma unroll
;                             for (int ks = 0; ks < 2; ++ks) { const bf16x8 ak = (MODE != 3) ? akf[kt][ks] : akq[kt][ks];
;                                 sc[kt] = __builtin_amdgcn_mfma_f32_16x16x32_bf16(ak, Bq[qd][ks], sc[kt], 0, 0, 0); } }
;                         if (MODE == 3) {
; #pragma unroll
;                             for (int st = 0; st < 2; ++st)
; #pragma unroll
;                                 for (int dt = 0; dt < 4; ++dt) avq[st][dt] = *(const LAS bf16x8*)(L + LV + (16 * dt + n) * 128 + ((((4 * st + q) ^ n) & 7) << 4));
;                             __builtin_amdgcn_sched_barrier(0);
;                         }
;                         if (!far) {
;                             const LAS float* tp = (MODE == 2) ? biasd + hr * NT + (DOFF - tq + 31 + 16 * p0) + 64 * q : biasd + hr * NT + (DOFF - tq + p0) + 4 * q;
; #pragma unroll
;                             for (int kt = 0; kt < 4; ++kt)
; #pragma unroll
;                                 for (int r = 0; r < 4; ++r) sc[kt][r] += (MODE == 3) ? bia[kt][r] : ((MODE == 2) ? tp[256 * kt + 16 * r] : tp[16 * kt + r]);
;                         }
.LBB0_1153:
	v_mbcnt_lo_u32_b32 v106, -1, 0
	v_mbcnt_hi_u32_b32 v106, -1, v106
	s_add_i32 s0, s55, -13
	v_lshrrev_b32_e32 v107, 3, v106
	v_add_u32_e32 v107, s0, v107
	s_add_i32 s0, 0, 0x25080
	v_min_i32_e32 v107, s52, v107
	v_lshl_add_u32 v107, v107, 2, s0
	ds_read_b32 v107, v107
	s_waitcnt lgkmcnt(0)
	v_lshrrev_b32_e32 v106, 5, v107
	v_lshl_add_u32 v106, v106, 2, v157
	ds_read_b32 v106, v106
	s_waitcnt lgkmcnt(0)
	v_lshrrev_b32_e32 v106, v107, v106
	v_and_b32_e32 v106, 1, v106
	v_cmp_eq_u32_e64 s[90:91], 1, v106
	s_cmp_lt_i32 s67, 0
	s_cselect_b64 s[0:1], -1, 0
	s_cmp_gt_i32 s67, s15
	s_cselect_b64 s[2:3], -1, 0
	s_or_b64 s[0:1], s[0:1], s[2:3]
	s_and_b64 vcc, exec, s[0:1]
	s_waitcnt lgkmcnt(0)
	s_barrier
	s_cbranch_vccnz .LBB0_1175
	s_bfe_u32 s0, s90, 0x80000
	s_cmp_eq_u32 s0, 0
	s_cbranch_scc1 .LBB0_1175
	s_sub_i32 s1, s16, s67
	s_cmpk_lt_i32 s1, 0x316
	s_cselect_b64 s[2:3], -1, 0
	v_cndmask_b32_e64 v106, 0, 1, s[2:3]
	s_and_b32 s1, s0, 15
	s_cmp_eq_u32 s1, 0
	v_cmp_ne_u32_e64 s[2:3], 1, v106
	s_cbranch_scc1 .LBB0_1166
	ds_read_b128 v[106:109], v206
	ds_read_b128 v[110:113], v206 offset:2048
	ds_read_b128 v[126:129], v208
	ds_read_b128 v[114:117], v208 offset:2048
	ds_read_b128 v[118:121], v206 offset:4096
	ds_read_b128 v[122:125], v206 offset:6144
	ds_read_b128 v[134:137], v208 offset:4096
	ds_read_b128 v[130:133], v208 offset:6144
	s_and_b64 vcc, exec, s[2:3]
	s_cbranch_vccnz .LBB0_1160
	v_sub_u32_e32 v138, s67, v196
	v_lshl_add_u32 v138, v138, 2, v233
	v_add_u32_e32 v139, 0xffc, v138
	ds_read2_b32 v[168:169], v139 offset1:1
	ds_read2_b32 v[170:171], v139 offset0:2 offset1:3
	ds_read2_b32 v[172:173], v139 offset0:16 offset1:17
	ds_read2_b32 v[174:175], v139 offset0:18 offset1:19
	ds_read2_b32 v[176:177], v139 offset0:32 offset1:33
	ds_read2_b32 v[178:179], v139 offset0:34 offset1:35
	ds_read2_b32 v[180:181], v139 offset0:48 offset1:49
	ds_read2_b32 v[182:183], v139 offset0:50 offset1:51
.LBB0_1160:
	s_waitcnt lgkmcnt(7)
	v_mfma_f32_16x16x32_bf16 v[106:109], v[106:109], v[58:61], 0
	s_waitcnt lgkmcnt(5)
	v_mfma_f32_16x16x32_bf16 v[150:153], v[126:129], v[62:65], v[106:109]
	v_mfma_f32_16x16x32_bf16 v[106:109], v[110:113], v[58:61], 0
	s_waitcnt lgkmcnt(4)
	v_mfma_f32_16x16x32_bf16 v[146:149], v[114:117], v[62:65], v[106:109]
	s_waitcnt lgkmcnt(3)
	v_mfma_f32_16x16x32_bf16 v[106:109], v[118:121], v[58:61], 0
	s_waitcnt lgkmcnt(1)
	v_mfma_f32_16x16x32_bf16 v[142:145], v[134:137], v[62:65], v[106:109]
	v_mfma_f32_16x16x32_bf16 v[106:109], v[122:125], v[58:61], 0
	s_waitcnt lgkmcnt(0)
	v_mfma_f32_16x16x32_bf16 v[110:113], v[130:133], v[62:65], v[106:109]
	ds_read_b128 v[138:141], v206 offset:8192
	ds_read_b128 v[134:137], v206 offset:10240
	ds_read_b128 v[130:133], v206 offset:12288
	ds_read_b128 v[126:129], v206 offset:14336
	ds_read_b128 v[122:125], v208 offset:8192
	ds_read_b128 v[118:121], v208 offset:10240
	ds_read_b128 v[114:117], v208 offset:12288
	ds_read_b128 v[106:109], v208 offset:14336
	s_and_b64 vcc, exec, s[2:3]
	s_cbranch_vccnz .LBB0_1162
	v_pk_add_f32 v[152:153], v[170:171], v[152:153]
	v_pk_add_f32 v[150:151], v[168:169], v[150:151]
	v_pk_add_f32 v[148:149], v[174:175], v[148:149]
	v_pk_add_f32 v[146:147], v[172:173], v[146:147]
	v_pk_add_f32 v[144:145], v[178:179], v[144:145]
	v_pk_add_f32 v[142:143], v[176:177], v[142:143]
	v_pk_add_f32 v[112:113], v[182:183], v[112:113]
	v_pk_add_f32 v[110:111], v[180:181], v[110:111]
	v_mov_b32_e32 v237, 0
	s_branch .LBB0_1163

; #define LAS __attribute__((address_space(3)))
;     ...
;                         if (MODE == 3) {
; #pragma unroll
;                             for (int kt = 0; kt < 4; ++kt)
; #pragma unroll
;                                 for (int ks = 0; ks < 2; ++ks) akq[kt][ks] = *(const LAS bf16x8*)(L + LK + (16 * kt + n) * 128 + ((((4 * ks + q) ^ n) & 7) << 4));
;                             if (!far) { const LAS float* tp = biasd + hr * NT + (DOFF - tq + p0) + 4 * q;
; #pragma unroll
;                                 for (int kt = 0; kt < 4; ++kt)
; #pragma unroll
;                                     for (int r = 0; r < 4; ++r) bia[kt][r] = tp[16 * kt + r]; }
;                             __builtin_amdgcn_sched_barrier(0);
;                         }
; #pragma unroll
;                         for (int kt = 0; kt < 4; ++kt) { sc[kt] = (f32x4){0.f, 0.f, 0.f, 0.f};
; #pragma unroll
;                             for (int ks = 0; ks < 2; ++ks) { const bf16x8 ak = (MODE != 3) ? akf[kt][ks] : akq[kt][ks];
;                                 sc[kt] = __builtin_amdgcn_mfma_f32_16x16x32_bf16(ak, Bq[qd][ks], sc[kt], 0, 0, 0); } }
;                         if (MODE == 3) {
; #pragma unroll
;                             for (int st = 0; st < 2; ++st)
; #pragma unroll
;                                 for (int dt = 0; dt < 4; ++dt) avq[st][dt] = *(const LAS bf16x8*)(L + LV + (16 * dt + n) * 128 + ((((4 * st + q) ^ n) & 7) << 4));
;                             __builtin_amdgcn_sched_barrier(0);
;                         }
;                         if (!far) {
;                             const LAS float* tp = (MODE == 2) ? biasd + hr * NT + (DOFF - tq + 31 + 16 * p0) + 64 * q : biasd + hr * NT + (DOFF - tq + p0) + 4 * q;
; #pragma unroll
;                             for (int kt = 0; kt < 4; ++kt)
; #pragma unroll
;                                 for (int r = 0; r < 4; ++r) sc[kt][r] += (MODE == 3) ? bia[kt][r] : ((MODE == 2) ? tp[256 * kt + 16 * r] : tp[16 * kt + r]);
;                         }
.LBB0_1166:
	s_and_b32 s1, s0, 0xf0
	s_cmp_eq_u32 s1, 0
	s_cbranch_scc1 .LBB0_1175
	ds_read_b128 v[106:109], v206
	ds_read_b128 v[110:113], v206 offset:2048
	ds_read_b128 v[126:129], v208
	ds_read_b128 v[114:117], v208 offset:2048
	ds_read_b128 v[118:121], v206 offset:4096
	ds_read_b128 v[122:125], v206 offset:6144
	ds_read_b128 v[134:137], v208 offset:4096
	ds_read_b128 v[130:133], v208 offset:6144
	s_and_b64 vcc, exec, s[2:3]
	s_cbranch_vccnz .LBB0_1169
	v_sub_u32_e32 v138, s67, v184
	v_lshl_add_u32 v138, v138, 2, v233
	v_add_u32_e32 v139, 0xffc, v138
	ds_read2_b32 v[168:169], v139 offset1:1
	ds_read2_b32 v[170:171], v139 offset0:2 offset1:3
	ds_read2_b32 v[172:173], v139 offset0:16 offset1:17
	ds_read2_b32 v[174:175], v139 offset0:18 offset1:19
	ds_read2_b32 v[176:177], v139 offset0:32 offset1:33
	ds_read2_b32 v[178:179], v139 offset0:34 offset1:35
	ds_read2_b32 v[180:181], v139 offset0:48 offset1:49
	ds_read2_b32 v[182:183], v139 offset0:50 offset1:51
.LBB0_1169:
	s_waitcnt lgkmcnt(7)
	v_mfma_f32_16x16x32_bf16 v[106:109], v[106:109], v[66:69], 0
	s_waitcnt lgkmcnt(5)
	v_mfma_f32_16x16x32_bf16 v[150:153], v[126:129], v[70:73], v[106:109]
	v_mfma_f32_16x16x32_bf16 v[106:109], v[110:113], v[66:69], 0
	s_waitcnt lgkmcnt(4)
	v_mfma_f32_16x16x32_bf16 v[146:149], v[114:117], v[70:73], v[106:109]
	s_waitcnt lgkmcnt(3)
	v_mfma_f32_16x16x32_bf16 v[106:109], v[118:121], v[66:69], 0
	s_waitcnt lgkmcnt(1)
	v_mfma_f32_16x16x32_bf16 v[142:145], v[134:137], v[70:73], v[106:109]
	v_mfma_f32_16x16x32_bf16 v[106:109], v[122:125], v[66:69], 0
	s_waitcnt lgkmcnt(0)
	v_mfma_f32_16x16x32_bf16 v[110:113], v[130:133], v[70:73], v[106:109]
	ds_read_b128 v[138:141], v206 offset:8192
	ds_read_b128 v[134:137], v206 offset:10240
	ds_read_b128 v[130:133], v206 offset:12288
	ds_read_b128 v[126:129], v206 offset:14336
	ds_read_b128 v[122:125], v208 offset:8192
	ds_read_b128 v[118:121], v208 offset:10240
	ds_read_b128 v[114:117], v208 offset:12288
	ds_read_b128 v[106:109], v208 offset:14336
	s_and_b64 vcc, exec, s[2:3]
	s_cbranch_vccnz .LBB0_1171
	v_pk_add_f32 v[152:153], v[170:171], v[152:153]
	v_pk_add_f32 v[150:151], v[168:169], v[150:151]
	v_pk_add_f32 v[148:149], v[174:175], v[148:149]
	v_pk_add_f32 v[146:147], v[172:173], v[146:147]
	v_pk_add_f32 v[144:145], v[178:179], v[144:145]
	v_pk_add_f32 v[142:143], v[176:177], v[142:143]
	v_pk_add_f32 v[112:113], v[182:183], v[112:113]
	v_pk_add_f32 v[110:111], v[180:181], v[110:111]
	v_mov_b32_e32 v237, 0
	s_branch .LBB0_1172

; #define LAS __attribute__((address_space(3)))
;     ...
;                         if (MODE == 3) {
; #pragma unroll
;                             for (int kt = 0; kt < 4; ++kt)
; #pragma unroll
;                                 for (int ks = 0; ks < 2; ++ks) akq[kt][ks] = *(const LAS bf16x8*)(L + LK + (16 * kt + n) * 128 + ((((4 * ks + q) ^ n) & 7) << 4));
;                             if (!far) { const LAS float* tp = biasd + hr * NT + (DOFF - tq + p0) + 4 * q;
; #pragma unroll
;                                 for (int kt = 0; kt < 4; ++kt)
; #pragma unroll
;                                     for (int r = 0; r < 4; ++r) bia[kt][r] = tp[16 * kt + r]; }
;                             __builtin_amdgcn_sched_barrier(0);
;                         }
; #pragma unroll
;                         for (int kt = 0; kt < 4; ++kt) { sc[kt] = (f32x4){0.f, 0.f, 0.f, 0.f};
; #pragma unroll
;                             for (int ks = 0; ks < 2; ++ks) { const bf16x8 ak = (MODE != 3) ? akf[kt][ks] : akq[kt][ks];
;                                 sc[kt] = __builtin_amdgcn_mfma_f32_16x16x32_bf16(ak, Bq[qd][ks], sc[kt], 0, 0, 0); } }
;                         if (MODE == 3) {
; #pragma unroll
;                             for (int st = 0; st < 2; ++st)
; #pragma unroll
;                                 for (int dt = 0; dt < 4; ++dt) avq[st][dt] = *(const LAS bf16x8*)(L + LV + (16 * dt + n) * 128 + ((((4 * st + q) ^ n) & 7) << 4));
;                             __builtin_amdgcn_sched_barrier(0);
;                         }
;                         if (!far) {
;                             const LAS float* tp = (MODE == 2) ? biasd + hr * NT + (DOFF - tq + 31 + 16 * p0) + 64 * q : biasd + hr * NT + (DOFF - tq + p0) + 4 * q;
; #pragma unroll
;                             for (int kt = 0; kt < 4; ++kt)
; #pragma unroll
;                                 for (int r = 0; r < 4; ++r) sc[kt][r] += (MODE == 3) ? bia[kt][r] : ((MODE == 2) ? tp[256 * kt + 16 * r] : tp[16 * kt + r]);
;                         }
.LBB0_1175:
	s_cmp_lt_i32 s66, 0
	s_cselect_b64 s[0:1], -1, 0
	s_cmp_gt_i32 s66, s15
	s_cselect_b64 s[2:3], -1, 0
	s_or_b64 s[0:1], s[0:1], s[2:3]
	s_and_b64 vcc, exec, s[0:1]
	s_cbranch_vccnz .LBB0_1197
	s_bfe_u32 s0, s90, 0x80008
	s_cmp_eq_u32 s0, 0
	s_cbranch_scc1 .LBB0_1197
	s_sub_i32 s1, s16, s66
	s_cmpk_lt_i32 s1, 0x316
	s_cselect_b64 s[2:3], -1, 0
	v_cndmask_b32_e64 v106, 0, 1, s[2:3]
	s_and_b32 s1, s0, 15
	s_cmp_eq_u32 s1, 0
	v_cmp_ne_u32_e64 s[2:3], 1, v106
	s_cbranch_scc1 .LBB0_1188
	ds_read_b128 v[106:109], v206 offset:16384
	ds_read_b128 v[110:113], v206 offset:18432
	ds_read_b128 v[126:129], v208 offset:16384
	ds_read_b128 v[114:117], v208 offset:18432
	ds_read_b128 v[118:121], v206 offset:20480
	ds_read_b128 v[122:125], v206 offset:22528
	ds_read_b128 v[134:137], v208 offset:20480
	ds_read_b128 v[130:133], v208 offset:22528
	s_and_b64 vcc, exec, s[2:3]
	s_cbranch_vccnz .LBB0_1182
	v_sub_u32_e32 v138, s66, v196
	v_lshl_add_u32 v138, v138, 2, v233
	v_add_u32_e32 v139, 0xffc, v138
	ds_read2_b32 v[168:169], v139 offset1:1
	ds_read2_b32 v[170:171], v139 offset0:2 offset1:3
	ds_read2_b32 v[172:173], v139 offset0:16 offset1:17
	ds_read2_b32 v[174:175], v139 offset0:18 offset1:19
	ds_read2_b32 v[176:177], v139 offset0:32 offset1:33
	ds_read2_b32 v[178:179], v139 offset0:34 offset1:35
	ds_read2_b32 v[180:181], v139 offset0:48 offset1:49
	ds_read2_b32 v[182:183], v139 offset0:50 offset1:51
.LBB0_1182:
	s_waitcnt lgkmcnt(7)
	v_mfma_f32_16x16x32_bf16 v[106:109], v[106:109], v[58:61], 0
	s_waitcnt lgkmcnt(5)
	v_mfma_f32_16x16x32_bf16 v[150:153], v[126:129], v[62:65], v[106:109]
	v_mfma_f32_16x16x32_bf16 v[106:109], v[110:113], v[58:61], 0
	s_waitcnt lgkmcnt(4)
	v_mfma_f32_16x16x32_bf16 v[146:149], v[114:117], v[62:65], v[106:109]
	s_waitcnt lgkmcnt(3)
	v_mfma_f32_16x16x32_bf16 v[106:109], v[118:121], v[58:61], 0
	s_waitcnt lgkmcnt(1)
	v_mfma_f32_16x16x32_bf16 v[142:145], v[134:137], v[62:65], v[106:109]
	v_mfma_f32_16x16x32_bf16 v[106:109], v[122:125], v[58:61], 0
	s_waitcnt lgkmcnt(0)
	v_mfma_f32_16x16x32_bf16 v[110:113], v[130:133], v[62:65], v[106:109]
	ds_read_b128 v[138:141], v206 offset:24576
	ds_read_b128 v[134:137], v206 offset:26624
	ds_read_b128 v[130:133], v206 offset:28672
	ds_read_b128 v[126:129], v206 offset:30720
	ds_read_b128 v[122:125], v208 offset:24576
	ds_read_b128 v[118:121], v208 offset:26624
	ds_read_b128 v[114:117], v208 offset:28672
	ds_read_b128 v[106:109], v208 offset:30720
	s_and_b64 vcc, exec, s[2:3]
	s_cbranch_vccnz .LBB0_1184
	v_pk_add_f32 v[152:153], v[170:171], v[152:153]
	v_pk_add_f32 v[150:151], v[168:169], v[150:151]
	v_pk_add_f32 v[148:149], v[174:175], v[148:149]
	v_pk_add_f32 v[146:147], v[172:173], v[146:147]
	v_pk_add_f32 v[144:145], v[178:179], v[144:145]
	v_pk_add_f32 v[142:143], v[176:177], v[142:143]
	v_pk_add_f32 v[112:113], v[182:183], v[112:113]
	v_pk_add_f32 v[110:111], v[180:181], v[110:111]
	v_mov_b32_e32 v237, 0
	s_branch .LBB0_1185

; #define LAS __attribute__((address_space(3)))
;     ...
;                         if (MODE == 3) {
; #pragma unroll
;                             for (int kt = 0; kt < 4; ++kt)
; #pragma unroll
;                                 for (int ks = 0; ks < 2; ++ks) akq[kt][ks] = *(const LAS bf16x8*)(L + LK + (16 * kt + n) * 128 + ((((4 * ks + q) ^ n) & 7) << 4));
;                             if (!far) { const LAS float* tp = biasd + hr * NT + (DOFF - tq + p0) + 4 * q;
; #pragma unroll
;                                 for (int kt = 0; kt < 4; ++kt)
; #pragma unroll
;                                     for (int r = 0; r < 4; ++r) bia[kt][r] = tp[16 * kt + r]; }
;                             __builtin_amdgcn_sched_barrier(0);
;                         }
; #pragma unroll
;                         for (int kt = 0; kt < 4; ++kt) { sc[kt] = (f32x4){0.f, 0.f, 0.f, 0.f};
; #pragma unroll
;                             for (int ks = 0; ks < 2; ++ks) { const bf16x8 ak = (MODE != 3) ? akf[kt][ks] : akq[kt][ks];
;                                 sc[kt] = __builtin_amdgcn_mfma_f32_16x16x32_bf16(ak, Bq[qd][ks], sc[kt], 0, 0, 0); } }
;                         if (MODE == 3) {
; #pragma unroll
;                             for (int st = 0; st < 2; ++st)
; #pragma unroll
;                                 for (int dt = 0; dt < 4; ++dt) avq[st][dt] = *(const LAS bf16x8*)(L + LV + (16 * dt + n) * 128 + ((((4 * st + q) ^ n) & 7) << 4));
;                             __builtin_amdgcn_sched_barrier(0);
;                         }
;                         if (!far) {
;                             const LAS float* tp = (MODE == 2) ? biasd + hr * NT + (DOFF - tq + 31 + 16 * p0) + 64 * q : biasd + hr * NT + (DOFF - tq + p0) + 4 * q;
; #pragma unroll
;                             for (int kt = 0; kt < 4; ++kt)
; #pragma unroll
;                                 for (int r = 0; r < 4; ++r) sc[kt][r] += (MODE == 3) ? bia[kt][r] : ((MODE == 2) ? tp[256 * kt + 16 * r] : tp[16 * kt + r]);
;                         }
.LBB0_1188:
	s_and_b32 s1, s0, 0xf0
	s_cmp_eq_u32 s1, 0
	s_cbranch_scc1 .LBB0_1197
	ds_read_b128 v[106:109], v206 offset:16384
	ds_read_b128 v[110:113], v206 offset:18432
	ds_read_b128 v[126:129], v208 offset:16384
	ds_read_b128 v[114:117], v208 offset:18432
	ds_read_b128 v[118:121], v206 offset:20480
	ds_read_b128 v[122:125], v206 offset:22528
	ds_read_b128 v[134:137], v208 offset:20480
	ds_read_b128 v[130:133], v208 offset:22528
	s_and_b64 vcc, exec, s[2:3]
	s_cbranch_vccnz .LBB0_1191
	v_sub_u32_e32 v138, s66, v184
	v_lshl_add_u32 v138, v138, 2, v233
	v_add_u32_e32 v139, 0xffc, v138
	ds_read2_b32 v[168:169], v139 offset1:1
	ds_read2_b32 v[170:171], v139 offset0:2 offset1:3
	ds_read2_b32 v[172:173], v139 offset0:16 offset1:17
	ds_read2_b32 v[174:175], v139 offset0:18 offset1:19
	ds_read2_b32 v[176:177], v139 offset0:32 offset1:33
	ds_read2_b32 v[178:179], v139 offset0:34 offset1:35
	ds_read2_b32 v[180:181], v139 offset0:48 offset1:49
	ds_read2_b32 v[182:183], v139 offset0:50 offset1:51
.LBB0_1191:
	s_waitcnt lgkmcnt(7)
	v_mfma_f32_16x16x32_bf16 v[106:109], v[106:109], v[66:69], 0
	s_waitcnt lgkmcnt(5)
	v_mfma_f32_16x16x32_bf16 v[150:153], v[126:129], v[70:73], v[106:109]
	v_mfma_f32_16x16x32_bf16 v[106:109], v[110:113], v[66:69], 0
	s_waitcnt lgkmcnt(4)
	v_mfma_f32_16x16x32_bf16 v[146:149], v[114:117], v[70:73], v[106:109]
	s_waitcnt lgkmcnt(3)
	v_mfma_f32_16x16x32_bf16 v[106:109], v[118:121], v[66:69], 0
	s_waitcnt lgkmcnt(1)
	v_mfma_f32_16x16x32_bf16 v[142:145], v[134:137], v[70:73], v[106:109]
	v_mfma_f32_16x16x32_bf16 v[106:109], v[122:125], v[66:69], 0
	s_waitcnt lgkmcnt(0)
	v_mfma_f32_16x16x32_bf16 v[110:113], v[130:133], v[70:73], v[106:109]
	ds_read_b128 v[138:141], v206 offset:24576
	ds_read_b128 v[134:137], v206 offset:26624
	ds_read_b128 v[130:133], v206 offset:28672
	ds_read_b128 v[126:129], v206 offset:30720
	ds_read_b128 v[122:125], v208 offset:24576
	ds_read_b128 v[118:121], v208 offset:26624
	ds_read_b128 v[114:117], v208 offset:28672
	ds_read_b128 v[106:109], v208 offset:30720
	s_and_b64 vcc, exec, s[2:3]
	s_cbranch_vccnz .LBB0_1193
	v_pk_add_f32 v[152:153], v[170:171], v[152:153]
	v_pk_add_f32 v[150:151], v[168:169], v[150:151]
	v_pk_add_f32 v[148:149], v[174:175], v[148:149]
	v_pk_add_f32 v[146:147], v[172:173], v[146:147]
	v_pk_add_f32 v[144:145], v[178:179], v[144:145]
	v_pk_add_f32 v[142:143], v[176:177], v[142:143]
	v_pk_add_f32 v[112:113], v[182:183], v[112:113]
	v_pk_add_f32 v[110:111], v[180:181], v[110:111]
	v_mov_b32_e32 v237, 0
	s_branch .LBB0_1194

; #define LAS __attribute__((address_space(3)))
;     ...
;                         if (MODE == 3) {
; #pragma unroll
;                             for (int kt = 0; kt < 4; ++kt)
; #pragma unroll
;                                 for (int ks = 0; ks < 2; ++ks) akq[kt][ks] = *(const LAS bf16x8*)(L + LK + (16 * kt + n) * 128 + ((((4 * ks + q) ^ n) & 7) << 4));
;                             if (!far) { const LAS float* tp = biasd + hr * NT + (DOFF - tq + p0) + 4 * q;
; #pragma unroll
;                                 for (int kt = 0; kt < 4; ++kt)
; #pragma unroll
;                                     for (int r = 0; r < 4; ++r) bia[kt][r] = tp[16 * kt + r]; }
;                             __builtin_amdgcn_sched_barrier(0);
;                         }
; #pragma unroll
;                         for (int kt = 0; kt < 4; ++kt) { sc[kt] = (f32x4){0.f, 0.f, 0.f, 0.f};
; #pragma unroll
;                             for (int ks = 0; ks < 2; ++ks) { const bf16x8 ak = (MODE != 3) ? akf[kt][ks] : akq[kt][ks];
;                                 sc[kt] = __builtin_amdgcn_mfma_f32_16x16x32_bf16(ak, Bq[qd][ks], sc[kt], 0, 0, 0); } }
;                         if (MODE == 3) {
; #pragma unroll
;                             for (int st = 0; st < 2; ++st)
; #pragma unroll
;                                 for (int dt = 0; dt < 4; ++dt) avq[st][dt] = *(const LAS bf16x8*)(L + LV + (16 * dt + n) * 128 + ((((4 * st + q) ^ n) & 7) << 4));
;                             __builtin_amdgcn_sched_barrier(0);
;                         }
;                         if (!far) {
;                             const LAS float* tp = (MODE == 2) ? biasd + hr * NT + (DOFF - tq + 31 + 16 * p0) + 64 * q : biasd + hr * NT + (DOFF - tq + p0) + 4 * q;
; #pragma unroll
;                             for (int kt = 0; kt < 4; ++kt)
; #pragma unroll
;                                 for (int r = 0; r < 4; ++r) sc[kt][r] += (MODE == 3) ? bia[kt][r] : ((MODE == 2) ? tp[256 * kt + 16 * r] : tp[16 * kt + r]);
;                         }
.LBB0_1197:
	s_cmp_lt_i32 s65, 0
	s_cselect_b64 s[0:1], -1, 0
	s_cmp_gt_i32 s65, s15
	s_cselect_b64 s[2:3], -1, 0
	s_or_b64 s[0:1], s[0:1], s[2:3]
	s_and_b64 vcc, exec, s[0:1]
	s_cbranch_vccnz .LBB0_1219
	s_bfe_u32 s0, s90, 0x80010
	s_cmp_eq_u32 s0, 0
	s_cbranch_scc1 .LBB0_1219
	s_sub_i32 s1, s16, s65
	s_cmpk_lt_i32 s1, 0x316
	s_cselect_b64 s[2:3], -1, 0
	v_cndmask_b32_e64 v106, 0, 1, s[2:3]
	s_and_b32 s1, s0, 15
	s_cmp_eq_u32 s1, 0
	v_cmp_ne_u32_e64 s[2:3], 1, v106
	s_cbranch_scc1 .LBB0_1210
	ds_read_b128 v[106:109], v206 offset:32768
	ds_read_b128 v[110:113], v206 offset:34816
	ds_read_b128 v[126:129], v208 offset:32768
	ds_read_b128 v[114:117], v208 offset:34816
	ds_read_b128 v[118:121], v206 offset:36864
	ds_read_b128 v[122:125], v206 offset:38912
	ds_read_b128 v[134:137], v208 offset:36864
	ds_read_b128 v[130:133], v208 offset:38912
	s_and_b64 vcc, exec, s[2:3]
	s_cbranch_vccnz .LBB0_1204
	v_sub_u32_e32 v138, s65, v196
	v_lshl_add_u32 v138, v138, 2, v233
	v_add_u32_e32 v139, 0xffc, v138
	ds_read2_b32 v[168:169], v139 offset1:1
	ds_read2_b32 v[170:171], v139 offset0:2 offset1:3
	ds_read2_b32 v[172:173], v139 offset0:16 offset1:17
	ds_read2_b32 v[174:175], v139 offset0:18 offset1:19
	ds_read2_b32 v[176:177], v139 offset0:32 offset1:33
	ds_read2_b32 v[178:179], v139 offset0:34 offset1:35
	ds_read2_b32 v[180:181], v139 offset0:48 offset1:49
	ds_read2_b32 v[182:183], v139 offset0:50 offset1:51
.LBB0_1204:
	s_waitcnt lgkmcnt(7)
	v_mfma_f32_16x16x32_bf16 v[106:109], v[106:109], v[58:61], 0
	s_waitcnt lgkmcnt(5)
	v_mfma_f32_16x16x32_bf16 v[150:153], v[126:129], v[62:65], v[106:109]
	v_mfma_f32_16x16x32_bf16 v[106:109], v[110:113], v[58:61], 0
	s_waitcnt lgkmcnt(4)
	v_mfma_f32_16x16x32_bf16 v[146:149], v[114:117], v[62:65], v[106:109]
	s_waitcnt lgkmcnt(3)
	v_mfma_f32_16x16x32_bf16 v[106:109], v[118:121], v[58:61], 0
	s_waitcnt lgkmcnt(1)
	v_mfma_f32_16x16x32_bf16 v[142:145], v[134:137], v[62:65], v[106:109]
	v_mfma_f32_16x16x32_bf16 v[106:109], v[122:125], v[58:61], 0
	s_waitcnt lgkmcnt(0)
	v_mfma_f32_16x16x32_bf16 v[110:113], v[130:133], v[62:65], v[106:109]
	ds_read_b128 v[138:141], v206 offset:40960
	ds_read_b128 v[134:137], v206 offset:43008
	ds_read_b128 v[130:133], v206 offset:45056
	ds_read_b128 v[126:129], v206 offset:47104
	ds_read_b128 v[122:125], v208 offset:40960
	ds_read_b128 v[118:121], v208 offset:43008
	ds_read_b128 v[114:117], v208 offset:45056
	ds_read_b128 v[106:109], v208 offset:47104
	s_and_b64 vcc, exec, s[2:3]
	s_cbranch_vccnz .LBB0_1206
	v_pk_add_f32 v[152:153], v[170:171], v[152:153]
	v_pk_add_f32 v[150:151], v[168:169], v[150:151]
	v_pk_add_f32 v[148:149], v[174:175], v[148:149]
	v_pk_add_f32 v[146:147], v[172:173], v[146:147]
	v_pk_add_f32 v[144:145], v[178:179], v[144:145]
	v_pk_add_f32 v[142:143], v[176:177], v[142:143]
	v_pk_add_f32 v[112:113], v[182:183], v[112:113]
	v_pk_add_f32 v[110:111], v[180:181], v[110:111]
	v_mov_b32_e32 v237, 0
	s_branch .LBB0_1207

; #define LAS __attribute__((address_space(3)))
;     ...
;                         if (MODE == 3) {
; #pragma unroll
;                             for (int kt = 0; kt < 4; ++kt)
; #pragma unroll
;                                 for (int ks = 0; ks < 2; ++ks) akq[kt][ks] = *(const LAS bf16x8*)(L + LK + (16 * kt + n) * 128 + ((((4 * ks + q) ^ n) & 7) << 4));
;                             if (!far) { const LAS float* tp = biasd + hr * NT + (DOFF - tq + p0) + 4 * q;
; #pragma unroll
;                                 for (int kt = 0; kt < 4; ++kt)
; #pragma unroll
;                                     for (int r = 0; r < 4; ++r) bia[kt][r] = tp[16 * kt + r]; }
;                             __builtin_amdgcn_sched_barrier(0);
;                         }
; #pragma unroll
;                         for (int kt = 0; kt < 4; ++kt) { sc[kt] = (f32x4){0.f, 0.f, 0.f, 0.f};
; #pragma unroll
;                             for (int ks = 0; ks < 2; ++ks) { const bf16x8 ak = (MODE != 3) ? akf[kt][ks] : akq[kt][ks];
;                                 sc[kt] = __builtin_amdgcn_mfma_f32_16x16x32_bf16(ak, Bq[qd][ks], sc[kt], 0, 0, 0); } }
;                         if (MODE == 3) {
; #pragma unroll
;                             for (int st = 0; st < 2; ++st)
; #pragma unroll
;                                 for (int dt = 0; dt < 4; ++dt) avq[st][dt] = *(const LAS bf16x8*)(L + LV + (16 * dt + n) * 128 + ((((4 * st + q) ^ n) & 7) << 4));
;                             __builtin_amdgcn_sched_barrier(0);
;                         }
;                         if (!far) {
;                             const LAS float* tp = (MODE == 2) ? biasd + hr * NT + (DOFF - tq + 31 + 16 * p0) + 64 * q : biasd + hr * NT + (DOFF - tq + p0) + 4 * q;
; #pragma unroll
;                             for (int kt = 0; kt < 4; ++kt)
; #pragma unroll
;                                 for (int r = 0; r < 4; ++r) sc[kt][r] += (MODE == 3) ? bia[kt][r] : ((MODE == 2) ? tp[256 * kt + 16 * r] : tp[16 * kt + r]);
;                         }
.LBB0_1210:
	s_and_b32 s1, s0, 0xf0
	s_cmp_eq_u32 s1, 0
	s_cbranch_scc1 .LBB0_1219
	ds_read_b128 v[106:109], v206 offset:32768
	ds_read_b128 v[110:113], v206 offset:34816
	ds_read_b128 v[126:129], v208 offset:32768
	ds_read_b128 v[114:117], v208 offset:34816
	ds_read_b128 v[118:121], v206 offset:36864
	ds_read_b128 v[122:125], v206 offset:38912
	ds_read_b128 v[134:137], v208 offset:36864
	ds_read_b128 v[130:133], v208 offset:38912
	s_and_b64 vcc, exec, s[2:3]
	s_cbranch_vccnz .LBB0_1213
	v_sub_u32_e32 v138, s65, v184
	v_lshl_add_u32 v138, v138, 2, v233
	v_add_u32_e32 v139, 0xffc, v138
	ds_read2_b32 v[168:169], v139 offset1:1
	ds_read2_b32 v[170:171], v139 offset0:2 offset1:3
	ds_read2_b32 v[172:173], v139 offset0:16 offset1:17
	ds_read2_b32 v[174:175], v139 offset0:18 offset1:19
	ds_read2_b32 v[176:177], v139 offset0:32 offset1:33
	ds_read2_b32 v[178:179], v139 offset0:34 offset1:35
	ds_read2_b32 v[180:181], v139 offset0:48 offset1:49
	ds_read2_b32 v[182:183], v139 offset0:50 offset1:51
.LBB0_1213:
	s_waitcnt lgkmcnt(7)
	v_mfma_f32_16x16x32_bf16 v[106:109], v[106:109], v[66:69], 0
	s_waitcnt lgkmcnt(5)
	v_mfma_f32_16x16x32_bf16 v[150:153], v[126:129], v[70:73], v[106:109]
	v_mfma_f32_16x16x32_bf16 v[106:109], v[110:113], v[66:69], 0
	s_waitcnt lgkmcnt(4)
	v_mfma_f32_16x16x32_bf16 v[146:149], v[114:117], v[70:73], v[106:109]
	s_waitcnt lgkmcnt(3)
	v_mfma_f32_16x16x32_bf16 v[106:109], v[118:121], v[66:69], 0
	s_waitcnt lgkmcnt(1)
	v_mfma_f32_16x16x32_bf16 v[142:145], v[134:137], v[70:73], v[106:109]
	v_mfma_f32_16x16x32_bf16 v[106:109], v[122:125], v[66:69], 0
	s_waitcnt lgkmcnt(0)
	v_mfma_f32_16x16x32_bf16 v[110:113], v[130:133], v[70:73], v[106:109]
	ds_read_b128 v[138:141], v206 offset:40960
	ds_read_b128 v[134:137], v206 offset:43008
	ds_read_b128 v[130:133], v206 offset:45056
	ds_read_b128 v[126:129], v206 offset:47104
	ds_read_b128 v[122:125], v208 offset:40960
	ds_read_b128 v[118:121], v208 offset:43008
	ds_read_b128 v[114:117], v208 offset:45056
	ds_read_b128 v[106:109], v208 offset:47104
	s_and_b64 vcc, exec, s[2:3]
	s_cbranch_vccnz .LBB0_1215
	v_pk_add_f32 v[152:153], v[170:171], v[152:153]
	v_pk_add_f32 v[150:151], v[168:169], v[150:151]
	v_pk_add_f32 v[148:149], v[174:175], v[148:149]
	v_pk_add_f32 v[146:147], v[172:173], v[146:147]
	v_pk_add_f32 v[144:145], v[178:179], v[144:145]
	v_pk_add_f32 v[142:143], v[176:177], v[142:143]
	v_pk_add_f32 v[112:113], v[182:183], v[112:113]
	v_pk_add_f32 v[110:111], v[180:181], v[110:111]
	v_mov_b32_e32 v237, 0
	s_branch .LBB0_1216

; #define LAS __attribute__((address_space(3)))
;     ...
;                         if (MODE == 3) {
; #pragma unroll
;                             for (int kt = 0; kt < 4; ++kt)
; #pragma unroll
;                                 for (int ks = 0; ks < 2; ++ks) akq[kt][ks] = *(const LAS bf16x8*)(L + LK + (16 * kt + n) * 128 + ((((4 * ks + q) ^ n) & 7) << 4));
;                             if (!far) { const LAS float* tp = biasd + hr * NT + (DOFF - tq + p0) + 4 * q;
; #pragma unroll
;                                 for (int kt = 0; kt < 4; ++kt)
; #pragma unroll
;                                     for (int r = 0; r < 4; ++r) bia[kt][r] = tp[16 * kt + r]; }
;                             __builtin_amdgcn_sched_barrier(0);
;                         }
; #pragma unroll
;                         for (int kt = 0; kt < 4; ++kt) { sc[kt] = (f32x4){0.f, 0.f, 0.f, 0.f};
; #pragma unroll
;                             for (int ks = 0; ks < 2; ++ks) { const bf16x8 ak = (MODE != 3) ? akf[kt][ks] : akq[kt][ks];
;                                 sc[kt] = __builtin_amdgcn_mfma_f32_16x16x32_bf16(ak, Bq[qd][ks], sc[kt], 0, 0, 0); } }
;                         if (MODE == 3) {
; #pragma unroll
;                             for (int st = 0; st < 2; ++st)
; #pragma unroll
;                                 for (int dt = 0; dt < 4; ++dt) avq[st][dt] = *(const LAS bf16x8*)(L + LV + (16 * dt + n) * 128 + ((((4 * st + q) ^ n) & 7) << 4));
;                             __builtin_amdgcn_sched_barrier(0);
;                         }
;                         if (!far) {
;                             const LAS float* tp = (MODE == 2) ? biasd + hr * NT + (DOFF - tq + 31 + 16 * p0) + 64 * q : biasd + hr * NT + (DOFF - tq + p0) + 4 * q;
; #pragma unroll
;                             for (int kt = 0; kt < 4; ++kt)
; #pragma unroll
;                                 for (int r = 0; r < 4; ++r) sc[kt][r] += (MODE == 3) ? bia[kt][r] : ((MODE == 2) ? tp[256 * kt + 16 * r] : tp[16 * kt + r]);
;                         }
.LBB0_1219:
	s_cmp_lt_i32 s64, 0
	s_cselect_b64 s[0:1], -1, 0
	s_cmp_gt_i32 s64, s15
	s_cselect_b64 s[2:3], -1, 0
	s_or_b64 s[0:1], s[0:1], s[2:3]
	s_and_b64 vcc, exec, s[0:1]
	s_cbranch_vccnz .LBB0_1241
	s_bfe_u32 s0, s90, 0x80018
	s_cmp_eq_u32 s0, 0
	s_cbranch_scc1 .LBB0_1241
	s_sub_i32 s1, s16, s64
	s_cmpk_lt_i32 s1, 0x316
	s_cselect_b64 s[2:3], -1, 0
	s_and_b32 s1, s0, 15
	v_cndmask_b32_e64 v106, 0, 1, s[2:3]
	s_cmp_eq_u32 s1, 0
	v_cmp_ne_u32_e64 s[2:3], 1, v106
	s_cbranch_scc1 .LBB0_1232
	ds_read_b128 v[106:109], v206 offset:49152
	ds_read_b128 v[110:113], v206 offset:51200
	ds_read_b128 v[126:129], v208 offset:49152
	ds_read_b128 v[114:117], v208 offset:51200
	ds_read_b128 v[118:121], v206 offset:53248
	ds_read_b128 v[122:125], v206 offset:55296
	ds_read_b128 v[134:137], v208 offset:53248
	ds_read_b128 v[130:133], v208 offset:55296
	s_and_b64 vcc, exec, s[2:3]
	s_cbranch_vccnz .LBB0_1226
	v_sub_u32_e32 v138, s64, v196
	v_lshl_add_u32 v138, v138, 2, v233
	v_add_u32_e32 v139, 0xffc, v138
	ds_read2_b32 v[168:169], v139 offset1:1
	ds_read2_b32 v[170:171], v139 offset0:2 offset1:3
	ds_read2_b32 v[172:173], v139 offset0:16 offset1:17
	ds_read2_b32 v[174:175], v139 offset0:18 offset1:19
	ds_read2_b32 v[176:177], v139 offset0:32 offset1:33
	ds_read2_b32 v[178:179], v139 offset0:34 offset1:35
	ds_read2_b32 v[180:181], v139 offset0:48 offset1:49
	ds_read2_b32 v[182:183], v139 offset0:50 offset1:51
.LBB0_1226:
	s_waitcnt lgkmcnt(7)
	v_mfma_f32_16x16x32_bf16 v[106:109], v[106:109], v[58:61], 0
	s_waitcnt lgkmcnt(5)
	v_mfma_f32_16x16x32_bf16 v[150:153], v[126:129], v[62:65], v[106:109]
	v_mfma_f32_16x16x32_bf16 v[106:109], v[110:113], v[58:61], 0
	s_waitcnt lgkmcnt(4)
	v_mfma_f32_16x16x32_bf16 v[146:149], v[114:117], v[62:65], v[106:109]
	s_waitcnt lgkmcnt(3)
	v_mfma_f32_16x16x32_bf16 v[106:109], v[118:121], v[58:61], 0
	s_waitcnt lgkmcnt(1)
	v_mfma_f32_16x16x32_bf16 v[142:145], v[134:137], v[62:65], v[106:109]
	v_mfma_f32_16x16x32_bf16 v[106:109], v[122:125], v[58:61], 0
	s_waitcnt lgkmcnt(0)
	v_mfma_f32_16x16x32_bf16 v[110:113], v[130:133], v[62:65], v[106:109]
	ds_read_b128 v[138:141], v206 offset:57344
	ds_read_b128 v[134:137], v206 offset:59392
	ds_read_b128 v[130:133], v206 offset:61440
	ds_read_b128 v[126:129], v206 offset:63488
	ds_read_b128 v[122:125], v208 offset:57344
	ds_read_b128 v[118:121], v208 offset:59392
	ds_read_b128 v[114:117], v208 offset:61440
	ds_read_b128 v[106:109], v208 offset:63488
	s_and_b64 vcc, exec, s[2:3]
	s_cbranch_vccnz .LBB0_1228
	v_pk_add_f32 v[152:153], v[170:171], v[152:153]
	v_pk_add_f32 v[150:151], v[168:169], v[150:151]
	v_pk_add_f32 v[148:149], v[174:175], v[148:149]
	v_pk_add_f32 v[146:147], v[172:173], v[146:147]
	v_pk_add_f32 v[144:145], v[178:179], v[144:145]
	v_pk_add_f32 v[142:143], v[176:177], v[142:143]
	v_pk_add_f32 v[112:113], v[182:183], v[112:113]
	v_pk_add_f32 v[110:111], v[180:181], v[110:111]
	v_mov_b32_e32 v239, 0
	s_branch .LBB0_1229

; #define LAS __attribute__((address_space(3)))
;     ...
;                         if (MODE == 3) {
; #pragma unroll
;                             for (int kt = 0; kt < 4; ++kt)
; #pragma unroll
;                                 for (int ks = 0; ks < 2; ++ks) akq[kt][ks] = *(const LAS bf16x8*)(L + LK + (16 * kt + n) * 128 + ((((4 * ks + q) ^ n) & 7) << 4));
;                             if (!far) { const LAS float* tp = biasd + hr * NT + (DOFF - tq + p0) + 4 * q;
; #pragma unroll
;                                 for (int kt = 0; kt < 4; ++kt)
; #pragma unroll
;                                     for (int r = 0; r < 4; ++r) bia[kt][r] = tp[16 * kt + r]; }
;                             __builtin_amdgcn_sched_barrier(0);
;                         }
; #pragma unroll
;                         for (int kt = 0; kt < 4; ++kt) { sc[kt] = (f32x4){0.f, 0.f, 0.f, 0.f};
; #pragma unroll
;                             for (int ks = 0; ks < 2; ++ks) { const bf16x8 ak = (MODE != 3) ? akf[kt][ks] : akq[kt][ks];
;                                 sc[kt] = __builtin_amdgcn_mfma_f32_16x16x32_bf16(ak, Bq[qd][ks], sc[kt], 0, 0, 0); } }
;                         if (MODE == 3) {
; #pragma unroll
;                             for (int st = 0; st < 2; ++st)
; #pragma unroll
;                                 for (int dt = 0; dt < 4; ++dt) avq[st][dt] = *(const LAS bf16x8*)(L + LV + (16 * dt + n) * 128 + ((((4 * st + q) ^ n) & 7) << 4));
;                             __builtin_amdgcn_sched_barrier(0);
;                         }
;                         if (!far) {
;                             const LAS float* tp = (MODE == 2) ? biasd + hr * NT + (DOFF - tq + 31 + 16 * p0) + 64 * q : biasd + hr * NT + (DOFF - tq + p0) + 4 * q;
; #pragma unroll
;                             for (int kt = 0; kt < 4; ++kt)
; #pragma unroll
;                                 for (int r = 0; r < 4; ++r) sc[kt][r] += (MODE == 3) ? bia[kt][r] : ((MODE == 2) ? tp[256 * kt + 16 * r] : tp[16 * kt + r]);
;                         }
.LBB0_1232:
	s_and_b32 s1, s0, 0xf0
	s_cmp_eq_u32 s1, 0
	s_cbranch_scc1 .LBB0_1241
	ds_read_b128 v[106:109], v206 offset:49152
	ds_read_b128 v[110:113], v206 offset:51200
	ds_read_b128 v[126:129], v208 offset:49152
	ds_read_b128 v[114:117], v208 offset:51200
	ds_read_b128 v[118:121], v206 offset:53248
	ds_read_b128 v[122:125], v206 offset:55296
	ds_read_b128 v[134:137], v208 offset:53248
	ds_read_b128 v[130:133], v208 offset:55296
	s_and_b64 vcc, exec, s[2:3]
	s_cbranch_vccnz .LBB0_1235
	v_sub_u32_e32 v138, s64, v184
	v_lshl_add_u32 v138, v138, 2, v233
	v_add_u32_e32 v139, 0xffc, v138
	ds_read2_b32 v[168:169], v139 offset1:1
	ds_read2_b32 v[170:171], v139 offset0:2 offset1:3
	ds_read2_b32 v[172:173], v139 offset0:16 offset1:17
	ds_read2_b32 v[174:175], v139 offset0:18 offset1:19
	ds_read2_b32 v[176:177], v139 offset0:32 offset1:33
	ds_read2_b32 v[178:179], v139 offset0:34 offset1:35
	ds_read2_b32 v[180:181], v139 offset0:48 offset1:49
	ds_read2_b32 v[182:183], v139 offset0:50 offset1:51
.LBB0_1235:
	s_waitcnt lgkmcnt(7)
	v_mfma_f32_16x16x32_bf16 v[106:109], v[106:109], v[66:69], 0
	s_waitcnt lgkmcnt(5)
	v_mfma_f32_16x16x32_bf16 v[150:153], v[126:129], v[70:73], v[106:109]
	v_mfma_f32_16x16x32_bf16 v[106:109], v[110:113], v[66:69], 0
	s_waitcnt lgkmcnt(4)
	v_mfma_f32_16x16x32_bf16 v[146:149], v[114:117], v[70:73], v[106:109]
	s_waitcnt lgkmcnt(3)
	v_mfma_f32_16x16x32_bf16 v[106:109], v[118:121], v[66:69], 0
	s_waitcnt lgkmcnt(1)
	v_mfma_f32_16x16x32_bf16 v[142:145], v[134:137], v[70:73], v[106:109]
	v_mfma_f32_16x16x32_bf16 v[106:109], v[122:125], v[66:69], 0
	s_waitcnt lgkmcnt(0)
	v_mfma_f32_16x16x32_bf16 v[110:113], v[130:133], v[70:73], v[106:109]
	ds_read_b128 v[138:141], v206 offset:57344
	ds_read_b128 v[134:137], v206 offset:59392
	ds_read_b128 v[130:133], v206 offset:61440
	ds_read_b128 v[126:129], v206 offset:63488
	ds_read_b128 v[122:125], v208 offset:57344
	ds_read_b128 v[118:121], v208 offset:59392
	ds_read_b128 v[114:117], v208 offset:61440
	ds_read_b128 v[106:109], v208 offset:63488
	s_and_b64 vcc, exec, s[2:3]
	s_cbranch_vccnz .LBB0_1237
	v_pk_add_f32 v[152:153], v[170:171], v[152:153]
	v_pk_add_f32 v[150:151], v[168:169], v[150:151]
	v_pk_add_f32 v[148:149], v[174:175], v[148:149]
	v_pk_add_f32 v[146:147], v[172:173], v[146:147]
	v_pk_add_f32 v[144:145], v[178:179], v[144:145]
	v_pk_add_f32 v[142:143], v[176:177], v[142:143]
	v_pk_add_f32 v[112:113], v[182:183], v[112:113]
	v_pk_add_f32 v[110:111], v[180:181], v[110:111]
	v_mov_b32_e32 v237, 0
	s_branch .LBB0_1238

; #define LAS __attribute__((address_space(3)))
;     ...
;                         if (MODE == 3) {
; #pragma unroll
;                             for (int kt = 0; kt < 4; ++kt)
; #pragma unroll
;                                 for (int ks = 0; ks < 2; ++ks) akq[kt][ks] = *(const LAS bf16x8*)(L + LK + (16 * kt + n) * 128 + ((((4 * ks + q) ^ n) & 7) << 4));
;                             if (!far) { const LAS float* tp = biasd + hr * NT + (DOFF - tq + p0) + 4 * q;
; #pragma unroll
;                                 for (int kt = 0; kt < 4; ++kt)
; #pragma unroll
;                                     for (int r = 0; r < 4; ++r) bia[kt][r] = tp[16 * kt + r]; }
;                             __builtin_amdgcn_sched_barrier(0);
;                         }
; #pragma unroll
;                         for (int kt = 0; kt < 4; ++kt) { sc[kt] = (f32x4){0.f, 0.f, 0.f, 0.f};
; #pragma unroll
;                             for (int ks = 0; ks < 2; ++ks) { const bf16x8 ak = (MODE != 3) ? akf[kt][ks] : akq[kt][ks];
;                                 sc[kt] = __builtin_amdgcn_mfma_f32_16x16x32_bf16(ak, Bq[qd][ks], sc[kt], 0, 0, 0); } }
;                         if (MODE == 3) {
; #pragma unroll
;                             for (int st = 0; st < 2; ++st)
; #pragma unroll
;                                 for (int dt = 0; dt < 4; ++dt) avq[st][dt] = *(const LAS bf16x8*)(L + LV + (16 * dt + n) * 128 + ((((4 * st + q) ^ n) & 7) << 4));
;                             __builtin_amdgcn_sched_barrier(0);
;                         }
;                         if (!far) {
;                             const LAS float* tp = (MODE == 2) ? biasd + hr * NT + (DOFF - tq + 31 + 16 * p0) + 64 * q : biasd + hr * NT + (DOFF - tq + p0) + 4 * q;
; #pragma unroll
;                             for (int kt = 0; kt < 4; ++kt)
; #pragma unroll
;                                 for (int r = 0; r < 4; ++r) sc[kt][r] += (MODE == 3) ? bia[kt][r] : ((MODE == 2) ? tp[256 * kt + 16 * r] : tp[16 * kt + r]);
;                         }
.LBB0_1241:
	s_cmp_lt_i32 s63, 0
	s_cselect_b64 s[0:1], -1, 0
	s_cmp_gt_i32 s63, s15
	s_cselect_b64 s[2:3], -1, 0
	s_or_b64 s[0:1], s[0:1], s[2:3]
	s_and_b64 vcc, exec, s[0:1]
	s_cbranch_vccnz .LBB0_1263
	s_bfe_u32 s0, s91, 0x80000
	s_cmp_eq_u32 s0, 0
	s_cbranch_scc1 .LBB0_1263
	s_sub_i32 s1, s16, s63
	s_cmpk_lt_i32 s1, 0x316
	s_cselect_b64 s[2:3], -1, 0
	s_and_b32 s1, s0, 15
	v_cndmask_b32_e64 v106, 0, 1, s[2:3]
	s_cmp_eq_u32 s1, 0
	v_cmp_ne_u32_e64 s[2:3], 1, v106
	s_cbranch_scc1 .LBB0_1254
	ds_read_b128 v[106:109], v209
	ds_read_b128 v[110:113], v210
	ds_read_b128 v[114:117], v209 offset:2048
	ds_read_b128 v[118:121], v210 offset:2048
	ds_read_b128 v[122:125], v209 offset:4096
	ds_read_b128 v[126:129], v210 offset:4096
	ds_read_b128 v[130:133], v209 offset:6144
	ds_read_b128 v[134:137], v210 offset:6144
	s_and_b64 vcc, exec, s[2:3]
	s_cbranch_vccnz .LBB0_1248
	v_sub_u32_e32 v138, s63, v196
	v_lshl_add_u32 v138, v138, 2, v233
	v_add_u32_e32 v139, 0xffc, v138
	ds_read2_b32 v[168:169], v139 offset1:1
	ds_read2_b32 v[170:171], v139 offset0:2 offset1:3
	ds_read2_b32 v[172:173], v139 offset0:16 offset1:17
	ds_read2_b32 v[174:175], v139 offset0:18 offset1:19
	ds_read2_b32 v[176:177], v139 offset0:32 offset1:33
	ds_read2_b32 v[178:179], v139 offset0:34 offset1:35
	ds_read2_b32 v[180:181], v139 offset0:48 offset1:49
	ds_read2_b32 v[182:183], v139 offset0:50 offset1:51
.LBB0_1248:
	s_waitcnt lgkmcnt(7)
	v_mfma_f32_16x16x32_bf16 v[106:109], v[106:109], v[58:61], 0
	s_waitcnt lgkmcnt(6)
	v_mfma_f32_16x16x32_bf16 v[150:153], v[110:113], v[62:65], v[106:109]
	s_waitcnt lgkmcnt(5)
	v_mfma_f32_16x16x32_bf16 v[106:109], v[114:117], v[58:61], 0
	s_waitcnt lgkmcnt(4)
	v_mfma_f32_16x16x32_bf16 v[146:149], v[118:121], v[62:65], v[106:109]
	s_waitcnt lgkmcnt(3)
	v_mfma_f32_16x16x32_bf16 v[106:109], v[122:125], v[58:61], 0
	s_waitcnt lgkmcnt(2)
	v_mfma_f32_16x16x32_bf16 v[142:145], v[126:129], v[62:65], v[106:109]
	s_waitcnt lgkmcnt(1)
	v_mfma_f32_16x16x32_bf16 v[106:109], v[130:133], v[58:61], 0
	s_waitcnt lgkmcnt(0)
	v_mfma_f32_16x16x32_bf16 v[106:109], v[134:137], v[62:65], v[106:109]
	ds_read_b128 v[138:141], v209 offset:8192
	ds_read_b128 v[130:133], v209 offset:10240
	ds_read_b128 v[134:137], v209 offset:12288
	ds_read_b128 v[126:129], v209 offset:14336
	ds_read_b128 v[122:125], v210 offset:8192
	ds_read_b128 v[118:121], v210 offset:10240
	ds_read_b128 v[114:117], v210 offset:12288
	ds_read_b128 v[110:113], v210 offset:14336
	s_and_b64 vcc, exec, s[2:3]
	s_cbranch_vccnz .LBB0_1250
	v_pk_add_f32 v[152:153], v[170:171], v[152:153]
	v_pk_add_f32 v[150:151], v[168:169], v[150:151]
	v_pk_add_f32 v[148:149], v[174:175], v[148:149]
	v_pk_add_f32 v[146:147], v[172:173], v[146:147]
	v_pk_add_f32 v[144:145], v[178:179], v[144:145]
	v_pk_add_f32 v[142:143], v[176:177], v[142:143]
	v_pk_add_f32 v[108:109], v[182:183], v[108:109]
	v_pk_add_f32 v[106:107], v[180:181], v[106:107]
	v_mov_b32_e32 v248, 0
	s_branch .LBB0_1251

; #define LAS __attribute__((address_space(3)))
;     ...
;                         if (MODE == 3) {
; #pragma unroll
;                             for (int kt = 0; kt < 4; ++kt)
; #pragma unroll
;                                 for (int ks = 0; ks < 2; ++ks) akq[kt][ks] = *(const LAS bf16x8*)(L + LK + (16 * kt + n) * 128 + ((((4 * ks + q) ^ n) & 7) << 4));
;                             if (!far) { const LAS float* tp = biasd + hr * NT + (DOFF - tq + p0) + 4 * q;
; #pragma unroll
;                                 for (int kt = 0; kt < 4; ++kt)
; #pragma unroll
;                                     for (int r = 0; r < 4; ++r) bia[kt][r] = tp[16 * kt + r]; }
;                             __builtin_amdgcn_sched_barrier(0);
;                         }
; #pragma unroll
;                         for (int kt = 0; kt < 4; ++kt) { sc[kt] = (f32x4){0.f, 0.f, 0.f, 0.f};
; #pragma unroll
;                             for (int ks = 0; ks < 2; ++ks) { const bf16x8 ak = (MODE != 3) ? akf[kt][ks] : akq[kt][ks];
;                                 sc[kt] = __builtin_amdgcn_mfma_f32_16x16x32_bf16(ak, Bq[qd][ks], sc[kt], 0, 0, 0); } }
;                         if (MODE == 3) {
; #pragma unroll
;                             for (int st = 0; st < 2; ++st)
; #pragma unroll
;                                 for (int dt = 0; dt < 4; ++dt) avq[st][dt] = *(const LAS bf16x8*)(L + LV + (16 * dt + n) * 128 + ((((4 * st + q) ^ n) & 7) << 4));
;                             __builtin_amdgcn_sched_barrier(0);
;                         }
;                         if (!far) {
;                             const LAS float* tp = (MODE == 2) ? biasd + hr * NT + (DOFF - tq + 31 + 16 * p0) + 64 * q : biasd + hr * NT + (DOFF - tq + p0) + 4 * q;
; #pragma unroll
;                             for (int kt = 0; kt < 4; ++kt)
; #pragma unroll
;                                 for (int r = 0; r < 4; ++r) sc[kt][r] += (MODE == 3) ? bia[kt][r] : ((MODE == 2) ? tp[256 * kt + 16 * r] : tp[16 * kt + r]);
;                         }
.LBB0_1254:
	s_and_b32 s1, s0, 0xf0
	s_cmp_eq_u32 s1, 0
	s_cbranch_scc1 .LBB0_1263
	ds_read_b128 v[106:109], v209
	ds_read_b128 v[110:113], v210
	ds_read_b128 v[114:117], v209 offset:2048
	ds_read_b128 v[118:121], v210 offset:2048
	ds_read_b128 v[122:125], v209 offset:4096
	ds_read_b128 v[126:129], v210 offset:4096
	ds_read_b128 v[130:133], v209 offset:6144
	ds_read_b128 v[134:137], v210 offset:6144
	s_and_b64 vcc, exec, s[2:3]
	s_cbranch_vccnz .LBB0_1257
	v_sub_u32_e32 v138, s63, v184
	v_lshl_add_u32 v138, v138, 2, v233
	v_add_u32_e32 v139, 0xffc, v138
	ds_read2_b32 v[168:169], v139 offset1:1
	ds_read2_b32 v[170:171], v139 offset0:2 offset1:3
	ds_read2_b32 v[172:173], v139 offset0:16 offset1:17
	ds_read2_b32 v[174:175], v139 offset0:18 offset1:19
	ds_read2_b32 v[176:177], v139 offset0:32 offset1:33
	ds_read2_b32 v[178:179], v139 offset0:34 offset1:35
	ds_read2_b32 v[180:181], v139 offset0:48 offset1:49
	ds_read2_b32 v[182:183], v139 offset0:50 offset1:51
.LBB0_1257:
	s_waitcnt lgkmcnt(7)
	v_mfma_f32_16x16x32_bf16 v[106:109], v[106:109], v[66:69], 0
	s_waitcnt lgkmcnt(6)
	v_mfma_f32_16x16x32_bf16 v[150:153], v[110:113], v[70:73], v[106:109]
	s_waitcnt lgkmcnt(5)
	v_mfma_f32_16x16x32_bf16 v[106:109], v[114:117], v[66:69], 0
	s_waitcnt lgkmcnt(4)
	v_mfma_f32_16x16x32_bf16 v[146:149], v[118:121], v[70:73], v[106:109]
	s_waitcnt lgkmcnt(3)
	v_mfma_f32_16x16x32_bf16 v[106:109], v[122:125], v[66:69], 0
	s_waitcnt lgkmcnt(2)
	v_mfma_f32_16x16x32_bf16 v[142:145], v[126:129], v[70:73], v[106:109]
	s_waitcnt lgkmcnt(1)
	v_mfma_f32_16x16x32_bf16 v[106:109], v[130:133], v[66:69], 0
	s_waitcnt lgkmcnt(0)
	v_mfma_f32_16x16x32_bf16 v[106:109], v[134:137], v[70:73], v[106:109]
	ds_read_b128 v[138:141], v209 offset:8192
	ds_read_b128 v[130:133], v209 offset:10240
	ds_read_b128 v[134:137], v209 offset:12288
	ds_read_b128 v[126:129], v209 offset:14336
	ds_read_b128 v[122:125], v210 offset:8192
	ds_read_b128 v[118:121], v210 offset:10240
	ds_read_b128 v[114:117], v210 offset:12288
	ds_read_b128 v[110:113], v210 offset:14336
	s_and_b64 vcc, exec, s[2:3]
	s_cbranch_vccnz .LBB0_1259
	v_pk_add_f32 v[152:153], v[170:171], v[152:153]
	v_pk_add_f32 v[150:151], v[168:169], v[150:151]
	v_pk_add_f32 v[148:149], v[174:175], v[148:149]
	v_pk_add_f32 v[146:147], v[172:173], v[146:147]
	v_pk_add_f32 v[144:145], v[178:179], v[144:145]
	v_pk_add_f32 v[142:143], v[176:177], v[142:143]
	v_pk_add_f32 v[108:109], v[182:183], v[108:109]
	v_pk_add_f32 v[106:107], v[180:181], v[106:107]
	v_mov_b32_e32 v237, 0
	s_branch .LBB0_1260

; #define LAS __attribute__((address_space(3)))
;     ...
;                         if (MODE == 3) {
; #pragma unroll
;                             for (int kt = 0; kt < 4; ++kt)
; #pragma unroll
;                                 for (int ks = 0; ks < 2; ++ks) akq[kt][ks] = *(const LAS bf16x8*)(L + LK + (16 * kt + n) * 128 + ((((4 * ks + q) ^ n) & 7) << 4));
;                             if (!far) { const LAS float* tp = biasd + hr * NT + (DOFF - tq + p0) + 4 * q;
; #pragma unroll
;                                 for (int kt = 0; kt < 4; ++kt)
; #pragma unroll
;                                     for (int r = 0; r < 4; ++r) bia[kt][r] = tp[16 * kt + r]; }
;                             __builtin_amdgcn_sched_barrier(0);
;                         }
; #pragma unroll
;                         for (int kt = 0; kt < 4; ++kt) { sc[kt] = (f32x4){0.f, 0.f, 0.f, 0.f};
; #pragma unroll
;                             for (int ks = 0; ks < 2; ++ks) { const bf16x8 ak = (MODE != 3) ? akf[kt][ks] : akq[kt][ks];
;                                 sc[kt] = __builtin_amdgcn_mfma_f32_16x16x32_bf16(ak, Bq[qd][ks], sc[kt], 0, 0, 0); } }
;                         if (MODE == 3) {
; #pragma unroll
;                             for (int st = 0; st < 2; ++st)
; #pragma unroll
;                                 for (int dt = 0; dt < 4; ++dt) avq[st][dt] = *(const LAS bf16x8*)(L + LV + (16 * dt + n) * 128 + ((((4 * st + q) ^ n) & 7) << 4));
;                             __builtin_amdgcn_sched_barrier(0);
;                         }
;                         if (!far) {
;                             const LAS float* tp = (MODE == 2) ? biasd + hr * NT + (DOFF - tq + 31 + 16 * p0) + 64 * q : biasd + hr * NT + (DOFF - tq + p0) + 4 * q;
; #pragma unroll
;                             for (int kt = 0; kt < 4; ++kt)
; #pragma unroll
;                                 for (int r = 0; r < 4; ++r) sc[kt][r] += (MODE == 3) ? bia[kt][r] : ((MODE == 2) ? tp[256 * kt + 16 * r] : tp[16 * kt + r]);
;                         }
.LBB0_1263:
	s_cmp_lt_i32 s53, 0
	s_cselect_b64 s[0:1], -1, 0
	s_cmp_gt_i32 s53, s15
	s_cselect_b64 s[2:3], -1, 0
	s_or_b64 s[0:1], s[0:1], s[2:3]
	s_and_b64 vcc, exec, s[0:1]
	s_cbranch_vccnz .LBB0_1285
	s_bfe_u32 s0, s91, 0x80008
	s_cmp_eq_u32 s0, 0
	s_cbranch_scc1 .LBB0_1285
	s_sub_i32 s1, s16, s53
	s_cmpk_lt_i32 s1, 0x316
	s_cselect_b64 s[2:3], -1, 0
	s_and_b32 s1, s0, 15
	v_cndmask_b32_e64 v106, 0, 1, s[2:3]
	s_cmp_eq_u32 s1, 0
	v_cmp_ne_u32_e64 s[2:3], 1, v106
	s_cbranch_scc1 .LBB0_1276
	ds_read_b128 v[106:109], v209 offset:16384
	ds_read_b128 v[110:113], v210 offset:16384
	ds_read_b128 v[114:117], v209 offset:18432
	ds_read_b128 v[118:121], v210 offset:18432
	ds_read_b128 v[122:125], v209 offset:20480
	ds_read_b128 v[126:129], v210 offset:20480
	ds_read_b128 v[130:133], v209 offset:22528
	ds_read_b128 v[134:137], v210 offset:22528
	s_and_b64 vcc, exec, s[2:3]
	s_cbranch_vccnz .LBB0_1270
	v_sub_u32_e32 v138, s53, v196
	v_lshl_add_u32 v138, v138, 2, v233
	v_add_u32_e32 v139, 0xffc, v138
	ds_read2_b32 v[168:169], v139 offset1:1
	ds_read2_b32 v[170:171], v139 offset0:2 offset1:3
	ds_read2_b32 v[172:173], v139 offset0:16 offset1:17
	ds_read2_b32 v[174:175], v139 offset0:18 offset1:19
	ds_read2_b32 v[176:177], v139 offset0:32 offset1:33
	ds_read2_b32 v[178:179], v139 offset0:34 offset1:35
	ds_read2_b32 v[180:181], v139 offset0:48 offset1:49
	ds_read2_b32 v[182:183], v139 offset0:50 offset1:51
.LBB0_1270:
	s_waitcnt lgkmcnt(7)
	v_mfma_f32_16x16x32_bf16 v[106:109], v[106:109], v[58:61], 0
	s_waitcnt lgkmcnt(6)
	v_mfma_f32_16x16x32_bf16 v[150:153], v[110:113], v[62:65], v[106:109]
	s_waitcnt lgkmcnt(5)
	v_mfma_f32_16x16x32_bf16 v[106:109], v[114:117], v[58:61], 0
	s_waitcnt lgkmcnt(4)
	v_mfma_f32_16x16x32_bf16 v[146:149], v[118:121], v[62:65], v[106:109]
	s_waitcnt lgkmcnt(3)
	v_mfma_f32_16x16x32_bf16 v[106:109], v[122:125], v[58:61], 0
	s_waitcnt lgkmcnt(2)
	v_mfma_f32_16x16x32_bf16 v[142:145], v[126:129], v[62:65], v[106:109]
	s_waitcnt lgkmcnt(1)
	v_mfma_f32_16x16x32_bf16 v[106:109], v[130:133], v[58:61], 0
	s_waitcnt lgkmcnt(0)
	v_mfma_f32_16x16x32_bf16 v[106:109], v[134:137], v[62:65], v[106:109]
	ds_read_b128 v[138:141], v209 offset:24576
	ds_read_b128 v[130:133], v209 offset:26624
	ds_read_b128 v[134:137], v209 offset:28672
	ds_read_b128 v[126:129], v209 offset:30720
	ds_read_b128 v[122:125], v210 offset:24576
	ds_read_b128 v[118:121], v210 offset:26624
	ds_read_b128 v[114:117], v210 offset:28672
	ds_read_b128 v[110:113], v210 offset:30720
	s_and_b64 vcc, exec, s[2:3]
	s_cbranch_vccnz .LBB0_1272
	v_pk_add_f32 v[152:153], v[170:171], v[152:153]
	v_pk_add_f32 v[150:151], v[168:169], v[150:151]
	v_pk_add_f32 v[148:149], v[174:175], v[148:149]
	v_pk_add_f32 v[146:147], v[172:173], v[146:147]
	v_pk_add_f32 v[144:145], v[178:179], v[144:145]
	v_pk_add_f32 v[142:143], v[176:177], v[142:143]
	v_pk_add_f32 v[108:109], v[182:183], v[108:109]
	v_pk_add_f32 v[106:107], v[180:181], v[106:107]
	v_mov_b32_e32 v248, 0
	s_branch .LBB0_1273

; #define LAS __attribute__((address_space(3)))
;     ...
;                         if (MODE == 3) {
; #pragma unroll
;                             for (int kt = 0; kt < 4; ++kt)
; #pragma unroll
;                                 for (int ks = 0; ks < 2; ++ks) akq[kt][ks] = *(const LAS bf16x8*)(L + LK + (16 * kt + n) * 128 + ((((4 * ks + q) ^ n) & 7) << 4));
;                             if (!far) { const LAS float* tp = biasd + hr * NT + (DOFF - tq + p0) + 4 * q;
; #pragma unroll
;                                 for (int kt = 0; kt < 4; ++kt)
; #pragma unroll
;                                     for (int r = 0; r < 4; ++r) bia[kt][r] = tp[16 * kt + r]; }
;                             __builtin_amdgcn_sched_barrier(0);
;                         }
; #pragma unroll
;                         for (int kt = 0; kt < 4; ++kt) { sc[kt] = (f32x4){0.f, 0.f, 0.f, 0.f};
; #pragma unroll
;                             for (int ks = 0; ks < 2; ++ks) { const bf16x8 ak = (MODE != 3) ? akf[kt][ks] : akq[kt][ks];
;                                 sc[kt] = __builtin_amdgcn_mfma_f32_16x16x32_bf16(ak, Bq[qd][ks], sc[kt], 0, 0, 0); } }
;                         if (MODE == 3) {
; #pragma unroll
;                             for (int st = 0; st < 2; ++st)
; #pragma unroll
;                                 for (int dt = 0; dt < 4; ++dt) avq[st][dt] = *(const LAS bf16x8*)(L + LV + (16 * dt + n) * 128 + ((((4 * st + q) ^ n) & 7) << 4));
;                             __builtin_amdgcn_sched_barrier(0);
;                         }
;                         if (!far) {
;                             const LAS float* tp = (MODE == 2) ? biasd + hr * NT + (DOFF - tq + 31 + 16 * p0) + 64 * q : biasd + hr * NT + (DOFF - tq + p0) + 4 * q;
; #pragma unroll
;                             for (int kt = 0; kt < 4; ++kt)
; #pragma unroll
;                                 for (int r = 0; r < 4; ++r) sc[kt][r] += (MODE == 3) ? bia[kt][r] : ((MODE == 2) ? tp[256 * kt + 16 * r] : tp[16 * kt + r]);
;                         }
.LBB0_1276:
	s_and_b32 s1, s0, 0xf0
	s_cmp_eq_u32 s1, 0
	s_cbranch_scc1 .LBB0_1285
	ds_read_b128 v[106:109], v209 offset:16384
	ds_read_b128 v[110:113], v210 offset:16384
	ds_read_b128 v[114:117], v209 offset:18432
	ds_read_b128 v[118:121], v210 offset:18432
	ds_read_b128 v[122:125], v209 offset:20480
	ds_read_b128 v[126:129], v210 offset:20480
	ds_read_b128 v[130:133], v209 offset:22528
	ds_read_b128 v[134:137], v210 offset:22528
	s_and_b64 vcc, exec, s[2:3]
	s_cbranch_vccnz .LBB0_1279
	v_sub_u32_e32 v138, s53, v184
	v_lshl_add_u32 v138, v138, 2, v233
	v_add_u32_e32 v139, 0xffc, v138
	ds_read2_b32 v[168:169], v139 offset1:1
	ds_read2_b32 v[170:171], v139 offset0:2 offset1:3
	ds_read2_b32 v[172:173], v139 offset0:16 offset1:17
	ds_read2_b32 v[174:175], v139 offset0:18 offset1:19
	ds_read2_b32 v[176:177], v139 offset0:32 offset1:33
	ds_read2_b32 v[178:179], v139 offset0:34 offset1:35
	ds_read2_b32 v[180:181], v139 offset0:48 offset1:49
	ds_read2_b32 v[182:183], v139 offset0:50 offset1:51
.LBB0_1279:
	s_waitcnt lgkmcnt(7)
	v_mfma_f32_16x16x32_bf16 v[106:109], v[106:109], v[66:69], 0
	s_waitcnt lgkmcnt(6)
	v_mfma_f32_16x16x32_bf16 v[150:153], v[110:113], v[70:73], v[106:109]
	s_waitcnt lgkmcnt(5)
	v_mfma_f32_16x16x32_bf16 v[106:109], v[114:117], v[66:69], 0
	s_waitcnt lgkmcnt(4)
	v_mfma_f32_16x16x32_bf16 v[146:149], v[118:121], v[70:73], v[106:109]
	s_waitcnt lgkmcnt(3)
	v_mfma_f32_16x16x32_bf16 v[106:109], v[122:125], v[66:69], 0
	s_waitcnt lgkmcnt(2)
	v_mfma_f32_16x16x32_bf16 v[142:145], v[126:129], v[70:73], v[106:109]
	s_waitcnt lgkmcnt(1)
	v_mfma_f32_16x16x32_bf16 v[106:109], v[130:133], v[66:69], 0
	s_waitcnt lgkmcnt(0)
	v_mfma_f32_16x16x32_bf16 v[106:109], v[134:137], v[70:73], v[106:109]
	ds_read_b128 v[138:141], v209 offset:24576
	ds_read_b128 v[130:133], v209 offset:26624
	ds_read_b128 v[134:137], v209 offset:28672
	ds_read_b128 v[126:129], v209 offset:30720
	ds_read_b128 v[122:125], v210 offset:24576
	ds_read_b128 v[118:121], v210 offset:26624
	ds_read_b128 v[114:117], v210 offset:28672
	ds_read_b128 v[110:113], v210 offset:30720
	s_and_b64 vcc, exec, s[2:3]
	s_cbranch_vccnz .LBB0_1281
	v_pk_add_f32 v[152:153], v[170:171], v[152:153]
	v_pk_add_f32 v[150:151], v[168:169], v[150:151]
	v_pk_add_f32 v[148:149], v[174:175], v[148:149]
	v_pk_add_f32 v[146:147], v[172:173], v[146:147]
	v_pk_add_f32 v[144:145], v[178:179], v[144:145]
	v_pk_add_f32 v[142:143], v[176:177], v[142:143]
	v_pk_add_f32 v[108:109], v[182:183], v[108:109]
	v_pk_add_f32 v[106:107], v[180:181], v[106:107]
	v_mov_b32_e32 v237, 0
	s_branch .LBB0_1282

; #define LAS __attribute__((address_space(3)))
;     ...
;                         if (MODE == 3) {
; #pragma unroll
;                             for (int kt = 0; kt < 4; ++kt)
; #pragma unroll
;                                 for (int ks = 0; ks < 2; ++ks) akq[kt][ks] = *(const LAS bf16x8*)(L + LK + (16 * kt + n) * 128 + ((((4 * ks + q) ^ n) & 7) << 4));
;                             if (!far) { const LAS float* tp = biasd + hr * NT + (DOFF - tq + p0) + 4 * q;
; #pragma unroll
;                                 for (int kt = 0; kt < 4; ++kt)
; #pragma unroll
;                                     for (int r = 0; r < 4; ++r) bia[kt][r] = tp[16 * kt + r]; }
;                             __builtin_amdgcn_sched_barrier(0);
;                         }
; #pragma unroll
;                         for (int kt = 0; kt < 4; ++kt) { sc[kt] = (f32x4){0.f, 0.f, 0.f, 0.f};
; #pragma unroll
;                             for (int ks = 0; ks < 2; ++ks) { const bf16x8 ak = (MODE != 3) ? akf[kt][ks] : akq[kt][ks];
;                                 sc[kt] = __builtin_amdgcn_mfma_f32_16x16x32_bf16(ak, Bq[qd][ks], sc[kt], 0, 0, 0); } }
;                         if (MODE == 3) {
; #pragma unroll
;                             for (int st = 0; st < 2; ++st)
; #pragma unroll
;                                 for (int dt = 0; dt < 4; ++dt) avq[st][dt] = *(const LAS bf16x8*)(L + LV + (16 * dt + n) * 128 + ((((4 * st + q) ^ n) & 7) << 4));
;                             __builtin_amdgcn_sched_barrier(0);
;                         }
;                         if (!far) {
;                             const LAS float* tp = (MODE == 2) ? biasd + hr * NT + (DOFF - tq + 31 + 16 * p0) + 64 * q : biasd + hr * NT + (DOFF - tq + p0) + 4 * q;
; #pragma unroll
;                             for (int kt = 0; kt < 4; ++kt)
; #pragma unroll
;                                 for (int r = 0; r < 4; ++r) sc[kt][r] += (MODE == 3) ? bia[kt][r] : ((MODE == 2) ? tp[256 * kt + 16 * r] : tp[16 * kt + r]);
;                         }
.LBB0_1285:
	s_cmp_lt_i32 s29, 0
	s_cselect_b64 s[0:1], -1, 0
	s_cmp_gt_i32 s29, s15
	s_cselect_b64 s[2:3], -1, 0
	s_or_b64 s[0:1], s[0:1], s[2:3]
	s_and_b64 vcc, exec, s[0:1]
	s_cbranch_vccnz .LBB0_1307
	s_bfe_u32 s0, s91, 0x80010
	s_cmp_eq_u32 s0, 0
	s_cbranch_scc1 .LBB0_1307
	s_sub_i32 s1, s16, s29
	s_cmpk_lt_i32 s1, 0x316
	s_cselect_b64 s[2:3], -1, 0
	s_and_b32 s1, s0, 15
	v_cndmask_b32_e64 v106, 0, 1, s[2:3]
	s_cmp_eq_u32 s1, 0
	v_cmp_ne_u32_e64 s[2:3], 1, v106
	s_cbranch_scc1 .LBB0_1298
	ds_read_b128 v[106:109], v209 offset:32768
	ds_read_b128 v[110:113], v210 offset:32768
	ds_read_b128 v[114:117], v209 offset:34816
	ds_read_b128 v[118:121], v210 offset:34816
	ds_read_b128 v[122:125], v209 offset:36864
	ds_read_b128 v[126:129], v210 offset:36864
	ds_read_b128 v[130:133], v209 offset:38912
	ds_read_b128 v[134:137], v210 offset:38912
	s_and_b64 vcc, exec, s[2:3]
	s_cbranch_vccnz .LBB0_1292
	v_sub_u32_e32 v138, s29, v196
	v_lshl_add_u32 v138, v138, 2, v233
	v_add_u32_e32 v139, 0xffc, v138
	ds_read2_b32 v[168:169], v139 offset1:1
	ds_read2_b32 v[170:171], v139 offset0:2 offset1:3
	ds_read2_b32 v[172:173], v139 offset0:16 offset1:17
	ds_read2_b32 v[174:175], v139 offset0:18 offset1:19
	ds_read2_b32 v[176:177], v139 offset0:32 offset1:33
	ds_read2_b32 v[178:179], v139 offset0:34 offset1:35
	ds_read2_b32 v[180:181], v139 offset0:48 offset1:49
	ds_read2_b32 v[182:183], v139 offset0:50 offset1:51
.LBB0_1292:
	s_waitcnt lgkmcnt(7)
	v_mfma_f32_16x16x32_bf16 v[106:109], v[106:109], v[58:61], 0
	s_waitcnt lgkmcnt(6)
	v_mfma_f32_16x16x32_bf16 v[150:153], v[110:113], v[62:65], v[106:109]
	s_waitcnt lgkmcnt(5)
	v_mfma_f32_16x16x32_bf16 v[106:109], v[114:117], v[58:61], 0
	s_waitcnt lgkmcnt(4)
	v_mfma_f32_16x16x32_bf16 v[146:149], v[118:121], v[62:65], v[106:109]
	s_waitcnt lgkmcnt(3)
	v_mfma_f32_16x16x32_bf16 v[106:109], v[122:125], v[58:61], 0
	s_waitcnt lgkmcnt(2)
	v_mfma_f32_16x16x32_bf16 v[142:145], v[126:129], v[62:65], v[106:109]
	s_waitcnt lgkmcnt(1)
	v_mfma_f32_16x16x32_bf16 v[106:109], v[130:133], v[58:61], 0
	s_waitcnt lgkmcnt(0)
	v_mfma_f32_16x16x32_bf16 v[106:109], v[134:137], v[62:65], v[106:109]
	ds_read_b128 v[138:141], v209 offset:40960
	ds_read_b128 v[130:133], v209 offset:43008
	ds_read_b128 v[134:137], v209 offset:45056
	ds_read_b128 v[126:129], v209 offset:47104
	ds_read_b128 v[122:125], v210 offset:40960
	ds_read_b128 v[118:121], v210 offset:43008
	ds_read_b128 v[114:117], v210 offset:45056
	ds_read_b128 v[110:113], v210 offset:47104
	s_and_b64 vcc, exec, s[2:3]
	s_cbranch_vccnz .LBB0_1294
	v_pk_add_f32 v[152:153], v[170:171], v[152:153]
	v_pk_add_f32 v[150:151], v[168:169], v[150:151]
	v_pk_add_f32 v[148:149], v[174:175], v[148:149]
	v_pk_add_f32 v[146:147], v[172:173], v[146:147]
	v_pk_add_f32 v[144:145], v[178:179], v[144:145]
	v_pk_add_f32 v[142:143], v[176:177], v[142:143]
	v_pk_add_f32 v[108:109], v[182:183], v[108:109]
	v_pk_add_f32 v[106:107], v[180:181], v[106:107]
	v_mov_b32_e32 v248, 0
	s_branch .LBB0_1295

; #define LAS __attribute__((address_space(3)))
;     ...
;                         if (MODE == 3) {
; #pragma unroll
;                             for (int kt = 0; kt < 4; ++kt)
; #pragma unroll
;                                 for (int ks = 0; ks < 2; ++ks) akq[kt][ks] = *(const LAS bf16x8*)(L + LK + (16 * kt + n) * 128 + ((((4 * ks + q) ^ n) & 7) << 4));
;                             if (!far) { const LAS float* tp = biasd + hr * NT + (DOFF - tq + p0) + 4 * q;
; #pragma unroll
;                                 for (int kt = 0; kt < 4; ++kt)
; #pragma unroll
;                                     for (int r = 0; r < 4; ++r) bia[kt][r] = tp[16 * kt + r]; }
;                             __builtin_amdgcn_sched_barrier(0);
;                         }
; #pragma unroll
;                         for (int kt = 0; kt < 4; ++kt) { sc[kt] = (f32x4){0.f, 0.f, 0.f, 0.f};
; #pragma unroll
;                             for (int ks = 0; ks < 2; ++ks) { const bf16x8 ak = (MODE != 3) ? akf[kt][ks] : akq[kt][ks];
;                                 sc[kt] = __builtin_amdgcn_mfma_f32_16x16x32_bf16(ak, Bq[qd][ks], sc[kt], 0, 0, 0); } }
;                         if (MODE == 3) {
; #pragma unroll
;                             for (int st = 0; st < 2; ++st)
; #pragma unroll
;                                 for (int dt = 0; dt < 4; ++dt) avq[st][dt] = *(const LAS bf16x8*)(L + LV + (16 * dt + n) * 128 + ((((4 * st + q) ^ n) & 7) << 4));
;                             __builtin_amdgcn_sched_barrier(0);
;                         }
;                         if (!far) {
;                             const LAS float* tp = (MODE == 2) ? biasd + hr * NT + (DOFF - tq + 31 + 16 * p0) + 64 * q : biasd + hr * NT + (DOFF - tq + p0) + 4 * q;
; #pragma unroll
;                             for (int kt = 0; kt < 4; ++kt)
; #pragma unroll
;                                 for (int r = 0; r < 4; ++r) sc[kt][r] += (MODE == 3) ? bia[kt][r] : ((MODE == 2) ? tp[256 * kt + 16 * r] : tp[16 * kt + r]);
;                         }
.LBB0_1298:
	s_and_b32 s1, s0, 0xf0
	s_cmp_eq_u32 s1, 0
	s_cbranch_scc1 .LBB0_1307
	ds_read_b128 v[106:109], v209 offset:32768
	ds_read_b128 v[110:113], v210 offset:32768
	ds_read_b128 v[114:117], v209 offset:34816
	ds_read_b128 v[118:121], v210 offset:34816
	ds_read_b128 v[122:125], v209 offset:36864
	ds_read_b128 v[126:129], v210 offset:36864
	ds_read_b128 v[130:133], v209 offset:38912
	ds_read_b128 v[134:137], v210 offset:38912
	s_and_b64 vcc, exec, s[2:3]
	s_cbranch_vccnz .LBB0_1301
	v_sub_u32_e32 v138, s29, v184
	v_lshl_add_u32 v138, v138, 2, v233
	v_add_u32_e32 v139, 0xffc, v138
	ds_read2_b32 v[168:169], v139 offset1:1
	ds_read2_b32 v[170:171], v139 offset0:2 offset1:3
	ds_read2_b32 v[172:173], v139 offset0:16 offset1:17
	ds_read2_b32 v[174:175], v139 offset0:18 offset1:19
	ds_read2_b32 v[176:177], v139 offset0:32 offset1:33
	ds_read2_b32 v[178:179], v139 offset0:34 offset1:35
	ds_read2_b32 v[180:181], v139 offset0:48 offset1:49
	ds_read2_b32 v[182:183], v139 offset0:50 offset1:51
.LBB0_1301:
	s_waitcnt lgkmcnt(7)
	v_mfma_f32_16x16x32_bf16 v[106:109], v[106:109], v[66:69], 0
	s_waitcnt lgkmcnt(6)
	v_mfma_f32_16x16x32_bf16 v[150:153], v[110:113], v[70:73], v[106:109]
	s_waitcnt lgkmcnt(5)
	v_mfma_f32_16x16x32_bf16 v[106:109], v[114:117], v[66:69], 0
	s_waitcnt lgkmcnt(4)
	v_mfma_f32_16x16x32_bf16 v[146:149], v[118:121], v[70:73], v[106:109]
	s_waitcnt lgkmcnt(3)
	v_mfma_f32_16x16x32_bf16 v[106:109], v[122:125], v[66:69], 0
	s_waitcnt lgkmcnt(2)
	v_mfma_f32_16x16x32_bf16 v[142:145], v[126:129], v[70:73], v[106:109]
	s_waitcnt lgkmcnt(1)
	v_mfma_f32_16x16x32_bf16 v[106:109], v[130:133], v[66:69], 0
	s_waitcnt lgkmcnt(0)
	v_mfma_f32_16x16x32_bf16 v[106:109], v[134:137], v[70:73], v[106:109]
	ds_read_b128 v[138:141], v209 offset:40960
	ds_read_b128 v[130:133], v209 offset:43008
	ds_read_b128 v[134:137], v209 offset:45056
	ds_read_b128 v[126:129], v209 offset:47104
	ds_read_b128 v[122:125], v210 offset:40960
	ds_read_b128 v[118:121], v210 offset:43008
	ds_read_b128 v[114:117], v210 offset:45056
	ds_read_b128 v[110:113], v210 offset:47104
	s_and_b64 vcc, exec, s[2:3]
	s_cbranch_vccnz .LBB0_1303
	v_pk_add_f32 v[152:153], v[170:171], v[152:153]
	v_pk_add_f32 v[150:151], v[168:169], v[150:151]
	v_pk_add_f32 v[148:149], v[174:175], v[148:149]
	v_pk_add_f32 v[146:147], v[172:173], v[146:147]
	v_pk_add_f32 v[144:145], v[178:179], v[144:145]
	v_pk_add_f32 v[142:143], v[176:177], v[142:143]
	v_pk_add_f32 v[108:109], v[182:183], v[108:109]
	v_pk_add_f32 v[106:107], v[180:181], v[106:107]
	v_mov_b32_e32 v237, 0
	s_branch .LBB0_1304
